# c24: c23 plus an early L2 write-back started by the arriver that leaves 16 or 4 workgroups of its XCD outstanding at each grid barrier
# baseline (speedup 1.0000x reference)
.LBB0_150:
	s_or_b64 exec, exec, s[10:11]
	v_cvt_f32_u32_e32 v5, v3
	s_waitcnt vmcnt(0)
	v_readfirstlane_b32 s2, v4
	v_sub_u32_e32 v4, 0, v3
	v_rcp_iflag_f32_e32 v5, v5
	v_add_u32_e32 v6, s2, v2
	v_mul_f32_e32 v5, 0x4f7ffffe, v5
	v_cvt_u32_f32_e32 v5, v5
	v_mul_lo_u32 v2, v4, v5
	v_mul_hi_u32 v2, v5, v2
	v_add_u32_e32 v2, v5, v2
	v_mul_hi_u32 v2, v6, v2
	v_mul_lo_u32 v4, v2, v3
	v_sub_u32_e32 v4, v6, v4
	v_add_u32_e32 v5, 1, v2
	v_cmp_ge_u32_e32 vcc, v4, v3
	s_nop 1
	v_cndmask_b32_e32 v2, v2, v5, vcc
	v_sub_u32_e32 v5, v4, v3
	v_cndmask_b32_e32 v4, v4, v5, vcc
	v_add_u32_e32 v5, 1, v2
	v_cmp_ge_u32_e32 vcc, v4, v3
	v_add_u32_e32 v4, 1, v6
	s_nop 0
	v_cndmask_b32_e32 v2, v2, v5, vcc
	v_mul_lo_u32 v5, v3, v2
	v_add_u32_e32 v3, v5, v3
	v_cmp_ne_u32_e32 vcc, v4, v3
	s_and_saveexec_b64 s[2:3], vcc
	s_xor_b64 s[8:9], exec, s[2:3]
	s_cbranch_execz .LBB0_164
	s_waitcnt lgkmcnt(0)
	v_sub_u32_e32 v5, v3, v4
	v_cmp_eq_u32_e32 vcc, 16, v5
	s_cbranch_vccnz .Lbar_fl_1
	v_cmp_eq_u32_e32 vcc, 4, v5
	s_cbranch_vccz .Lbar_nofl_1
.Lbar_fl_1:
	buffer_wbl2 sc1
.Lbar_nofl_1:
	v_mov_b32_e32 v1, 0x7000
	global_load_dword v1, v1, s[50:51] offset:1280 sc1
	s_add_u32 s14, s50, 0x7500
	s_addc_u32 s15, s51, 0
	s_waitcnt vmcnt(0)
	v_cmp_eq_u32_e32 vcc, v1, v2
	s_and_saveexec_b64 s[10:11], vcc
	s_cbranch_execz .LBB0_163
	s_add_u32 s12, s50, 0x4200
	s_addc_u32 s13, s51, 0
	s_mov_b32 s2, 1
	s_mov_b64 s[16:17], 0
	v_mov_b32_e32 v1, 0
	s_branch .LBB0_154

.LBB0_1537:
	s_or_b64 exec, exec, s[10:11]
	v_cvt_f32_u32_e32 v4, v2
	s_waitcnt vmcnt(0)
	v_readfirstlane_b32 s2, v3
	v_sub_u32_e32 v3, 0, v2
	v_rcp_iflag_f32_e32 v4, v4
	v_add_u32_e32 v5, s2, v1
	v_mul_f32_e32 v4, 0x4f7ffffe, v4
	v_cvt_u32_f32_e32 v4, v4
	v_mul_lo_u32 v1, v3, v4
	v_mul_hi_u32 v1, v4, v1
	v_add_u32_e32 v1, v4, v1
	v_mul_hi_u32 v1, v5, v1
	v_mul_lo_u32 v3, v1, v2
	v_sub_u32_e32 v3, v5, v3
	v_add_u32_e32 v4, 1, v1
	v_cmp_ge_u32_e32 vcc, v3, v2
	s_nop 1
	v_cndmask_b32_e32 v1, v1, v4, vcc
	v_sub_u32_e32 v4, v3, v2
	v_cndmask_b32_e32 v3, v3, v4, vcc
	v_add_u32_e32 v4, 1, v1
	v_cmp_ge_u32_e32 vcc, v3, v2
	v_add_u32_e32 v3, 1, v5
	s_nop 0
	v_cndmask_b32_e32 v1, v1, v4, vcc
	v_mul_lo_u32 v4, v2, v1
	v_add_u32_e32 v2, v4, v2
	v_cmp_ne_u32_e32 vcc, v3, v2
	s_and_saveexec_b64 s[2:3], vcc
	s_xor_b64 s[8:9], exec, s[2:3]
	s_cbranch_execz .LBB0_1551
	s_waitcnt lgkmcnt(0)
	v_sub_u32_e32 v4, v2, v3
	v_cmp_eq_u32_e32 vcc, 16, v4
	s_cbranch_vccnz .Lbar_fl_9
	v_cmp_eq_u32_e32 vcc, 4, v4
	s_cbranch_vccz .Lbar_nofl_9

.Lbar_nofl_9:
	v_mov_b32_e32 v0, 0x7000
	global_load_dword v0, v0, s[50:51] offset:1280 sc1
	s_add_u32 s14, s50, 0x7500
	s_addc_u32 s15, s51, 0
	s_waitcnt vmcnt(0)
	v_cmp_eq_u32_e32 vcc, v0, v1
	s_and_saveexec_b64 s[10:11], vcc
	s_cbranch_execz .LBB0_1550
	s_add_u32 s12, s50, 0x4200
	s_addc_u32 s13, s51, 0
	s_mov_b32 s2, 1
	s_mov_b64 s[16:17], 0
	v_mov_b32_e32 v0, 0
	s_branch .LBB0_1541
